# exp_v: drop the redundant early vmcnt(16) before the first gather group
# baseline (speedup 1.0000x reference)
; #define EV_LOADN(q_, g0_, n_) _Pragma("unroll") for (int k = 0; k < (n_); ++k) q_[k] = __builtin_bit_cast(uint4, __builtin_amdgcn_raw_buffer_load_b128(vrs, voff + si[((g0_) + k) * 8 + sub] * 128, 0, GATHER_AUX))
; #define EV_WAIT(n_) asm volatile("s_waitcnt vmcnt(" #n_ ")" ::: "memory")
; __device__ void phase_exp_v(KParams& p, char* smem) {
;     ...
;       for (int tt = 0; tt < 16; ++tt) {
;         const int t = chunk * 64 + w * 16 + tt;
;         __builtin_amdgcn_wave_barrier();
;         si[lane] = e0n; si[64 + lane] = e1n;
;         sc[lane] = g0n; sc[64 + lane] = g1n;
;         __builtin_amdgcn_wave_barrier();
;         f32x2 acc[16];
; #pragma unroll
;         for (int e = 0; e < 16; ++e) acc[e] = f32x2{0.f, 0.f};
;         const __amdgpu_buffer_rsrc_t vrs = __builtin_amdgcn_make_buffer_rsrc((void*)p.V8, 0, 0x2000000, 0x00020000);
;         const int voff = (int)x * (16384 * 128) + cc * 16;
;         uint4 qa[4], qb[4], qc[4], qd[4];
;     ...
;         EV_LOADN(qa, 0, 4); EV_LOADN(qb, 4, 4); EV_LOADN(qc, 8, 4); EV_LOADN(qd, 12, 4);
;         {
;           const int t1 = (tt + 1 < 16) ? t + 1 : t;
;           e0n = p.idx[(size_t)t1 * 128 + lane]; e1n = p.idx[(size_t)t1 * 128 + 64 + lane];
;           g0n = p.gate[(size_t)t1 * 128 + lane]; g1n = p.gate[(size_t)t1 * 128 + 64 + lane];
;         }
;         EV_WAIT(16); EV_COMPN(qa, 0, 4);
.LBB0_1393:
	s_waitcnt vmcnt(3)
	ds_write2_b32 v54, v64, v65 offset0:16 offset1:80
	s_waitcnt vmcnt(1)
	ds_write2_b32 v54, v66, v67 offset0:144 offset1:208
	ds_read2_b32 v[200:201], v56 offset0:16 offset1:24
	ds_read2_b32 v[202:203], v56 offset0:32 offset1:40
	ds_read2_b32 v[204:205], v56 offset0:48 offset1:56
	ds_read2_b32 v[206:207], v56 offset0:64 offset1:72
	ds_read2_b32 v[208:209], v56 offset0:80 offset1:88
	ds_read2_b32 v[210:211], v56 offset0:96 offset1:104
	ds_read2_b32 v[212:213], v56 offset0:112 offset1:120
	ds_read2_b32 v[214:215], v56 offset0:128 offset1:136
	s_cmpk_lg_u32 s18, 0xf000
	s_cselect_b64 s[20:21], -1, 0
	v_cndmask_b32_e64 v64, 0, 1, s[20:21]
	v_mov_b32_e32 v65, s37
	v_lshl_add_u64 v[64:65], v[50:51], 0, v[64:65]
	v_lshlrev_b64 v[66:67], 9, v[64:65]
	v_lshl_or_b32 v66, v44, 2, v66
	v_lshl_add_u64 v[88:89], s[10:11], 0, v[66:67]
	v_lshl_add_u64 v[50:51], v[50:51], 0, 1
	s_waitcnt lgkmcnt(7)
	v_lshl_add_u32 v0, v200, 7, v63
	buffer_load_dwordx4 v[68:71], v0, s[12:15], 0 offen sc0
	v_lshl_add_u32 v0, v201, 7, v63
	buffer_load_dwordx4 v[72:75], v0, s[12:15], 0 offen sc0
	ds_read2_b32 v[216:217], v56 offset0:144 offset1:152
	s_waitcnt lgkmcnt(7)
	v_lshl_add_u32 v0, v202, 7, v63
	buffer_load_dwordx4 v[76:79], v0, s[12:15], 0 offen sc0
	v_lshl_add_u32 v0, v203, 7, v63
	buffer_load_dwordx4 v[80:83], v0, s[12:15], 0 offen sc0
	ds_read2_b32 v[218:219], v56 offset0:160 offset1:168
	s_waitcnt lgkmcnt(7)
	v_lshl_add_u32 v0, v204, 7, v63
	buffer_load_dwordx4 v[84:87], v0, s[12:15], 0 offen sc0
	v_lshl_add_u32 v0, v205, 7, v63
	buffer_load_dwordx4 v[40:43], v0, s[12:15], 0 offen sc0
	ds_read2_b32 v[220:221], v56 offset0:176 offset1:184
	s_waitcnt lgkmcnt(7)
	v_lshl_add_u32 v0, v206, 7, v63
	buffer_load_dwordx4 v[36:39], v0, s[12:15], 0 offen sc0
	v_lshl_add_u32 v0, v207, 7, v63
	buffer_load_dwordx4 v[32:35], v0, s[12:15], 0 offen sc0
	ds_read2_b32 v[222:223], v56 offset0:192 offset1:200
	s_waitcnt lgkmcnt(7)
	v_lshl_add_u32 v0, v208, 7, v63
	buffer_load_dwordx4 v[28:31], v0, s[12:15], 0 offen sc0
	v_lshl_add_u32 v0, v209, 7, v63
	buffer_load_dwordx4 v[24:27], v0, s[12:15], 0 offen sc0
	ds_read2_b32 v[224:225], v56 offset0:208 offset1:216
	s_waitcnt lgkmcnt(7)
	v_lshl_add_u32 v0, v210, 7, v63
	buffer_load_dwordx4 v[20:23], v0, s[12:15], 0 offen sc0
	v_lshl_add_u32 v0, v211, 7, v63
	buffer_load_dwordx4 v[16:19], v0, s[12:15], 0 offen sc0
	ds_read2_b32 v[226:227], v56 offset0:224 offset1:232
	s_waitcnt lgkmcnt(7)
	v_lshl_add_u32 v0, v212, 7, v63
	buffer_load_dwordx4 v[12:15], v0, s[12:15], 0 offen sc0
	v_lshl_add_u32 v0, v213, 7, v63
	buffer_load_dwordx4 v[8:11], v0, s[12:15], 0 offen sc0
	ds_read2_b32 v[228:229], v56 offset0:240 offset1:248
	ds_read2_b32 v[230:231], v61 offset1:8
	s_waitcnt lgkmcnt(8)
	v_lshl_add_u32 v0, v214, 7, v63
	buffer_load_dwordx4 v[4:7], v0, s[12:15], 0 offen sc0
	v_lshl_add_u32 v0, v215, 7, v63
	buffer_load_dwordx4 v[0:3], v0, s[12:15], 0 offen sc0
	s_nop 0
	global_load_dword v64, v[88:89], off
	global_load_dword v65, v[88:89], off offset:256
	v_lshl_add_u64 v[88:89], s[8:9], 0, v[66:67]
	global_load_dword v66, v[88:89], off
	global_load_dword v67, v[88:89], off offset:256
	s_waitcnt lgkmcnt(0)
	s_waitcnt vmcnt(19)
	v_cvt_scalef32_pk_f32_fp4 v[152:153], v68, 1.0
	v_cvt_scalef32_pk_f32_fp4 v[154:155], v68, 1.0 op_sel:[1,0,0]
	v_cvt_scalef32_pk_f32_fp4 v[156:157], v68, 1.0 op_sel:[0,1,0]
	v_cvt_scalef32_pk_f32_fp4 v[158:159], v68, 1.0 op_sel:[1,1,0]
	v_cvt_scalef32_pk_f32_fp4 v[160:161], v69, 1.0
	v_pk_mul_f32 v[120:121], v[216:217], v[152:153] op_sel_hi:[0,1]
	v_cvt_scalef32_pk_f32_fp4 v[162:163], v69, 1.0 op_sel:[1,0,0]
	v_pk_mul_f32 v[122:123], v[216:217], v[154:155] op_sel_hi:[0,1]
	v_cvt_scalef32_pk_f32_fp4 v[152:153], v69, 1.0 op_sel:[0,1,0]
	v_pk_mul_f32 v[124:125], v[216:217], v[156:157] op_sel_hi:[0,1]
	v_cvt_scalef32_pk_f32_fp4 v[154:155], v69, 1.0 op_sel:[1,1,0]
	v_pk_mul_f32 v[126:127], v[216:217], v[158:159] op_sel_hi:[0,1]
	v_cvt_scalef32_pk_f32_fp4 v[156:157], v70, 1.0
	v_pk_mul_f32 v[128:129], v[216:217], v[160:161] op_sel_hi:[0,1]
	v_cvt_scalef32_pk_f32_fp4 v[158:159], v70, 1.0 op_sel:[1,0,0]
	v_pk_mul_f32 v[130:131], v[216:217], v[162:163] op_sel_hi:[0,1]
	v_cvt_scalef32_pk_f32_fp4 v[160:161], v70, 1.0 op_sel:[0,1,0]
	v_pk_mul_f32 v[132:133], v[216:217], v[152:153] op_sel_hi:[0,1]
	v_cvt_scalef32_pk_f32_fp4 v[162:163], v70, 1.0 op_sel:[1,1,0]
	v_pk_mul_f32 v[134:135], v[216:217], v[154:155] op_sel_hi:[0,1]
	v_cvt_scalef32_pk_f32_fp4 v[152:153], v71, 1.0
	v_pk_mul_f32 v[136:137], v[216:217], v[156:157] op_sel_hi:[0,1]
	v_cvt_scalef32_pk_f32_fp4 v[154:155], v71, 1.0 op_sel:[1,0,0]
	v_pk_mul_f32 v[138:139], v[216:217], v[158:159] op_sel_hi:[0,1]
	v_cvt_scalef32_pk_f32_fp4 v[156:157], v71, 1.0 op_sel:[0,1,0]
	v_pk_mul_f32 v[140:141], v[216:217], v[160:161] op_sel_hi:[0,1]
	v_cvt_scalef32_pk_f32_fp4 v[158:159], v71, 1.0 op_sel:[1,1,0]
	v_pk_mul_f32 v[142:143], v[216:217], v[162:163] op_sel_hi:[0,1]
	v_pk_mul_f32 v[144:145], v[216:217], v[152:153] op_sel_hi:[0,1]
	v_pk_mul_f32 v[146:147], v[216:217], v[154:155] op_sel_hi:[0,1]
	v_pk_mul_f32 v[148:149], v[216:217], v[156:157] op_sel_hi:[0,1]
	v_pk_mul_f32 v[150:151], v[216:217], v[158:159] op_sel_hi:[0,1]
	s_waitcnt vmcnt(18)
; #define EV_LOADN(q_, g0_, n_) _Pragma("unroll") for (int k = 0; k < (n_); ++k) q_[k] = __builtin_bit_cast(uint4, __builtin_amdgcn_raw_buffer_load_b128(vrs, voff + si[((g0_) + k) * 8 + sub] * 128, 0, GATHER_AUX))
; #define EV_WAIT(n_) asm volatile("s_waitcnt vmcnt(" #n_ ")" ::: "memory")
; __device__ void phase_exp_v(KParams& p, char* smem) {
;     ...
;         EV_LOADN(qa, 0, 4); EV_LOADN(qb, 4, 4); EV_LOADN(qc, 8, 4); EV_LOADN(qd, 12, 4);
;         {
;           const int t1 = (tt + 1 < 16) ? t + 1 : t;
;           e0n = p.idx[(size_t)t1 * 128 + lane]; e1n = p.idx[(size_t)t1 * 128 + 64 + lane];
;           g0n = p.gate[(size_t)t1 * 128 + lane]; g1n = p.gate[(size_t)t1 * 128 + 64 + lane];
;         }
;         EV_WAIT(16); EV_COMPN(qa, 0, 4);
;         EV_WAIT(12); EV_COMPN(qb, 4, 4);
;         EV_WAIT(8); EV_COMPN(qc, 8, 4);
;         EV_WAIT(4); EV_COMPN(qd, 12, 4);
	v_cvt_scalef32_pk_f32_fp4 v[152:153], v72, 1.0
	v_cvt_scalef32_pk_f32_fp4 v[154:155], v72, 1.0 op_sel:[1,0,0]
	v_cvt_scalef32_pk_f32_fp4 v[156:157], v72, 1.0 op_sel:[0,1,0]
	v_cvt_scalef32_pk_f32_fp4 v[158:159], v72, 1.0 op_sel:[1,1,0]
	v_cvt_scalef32_pk_f32_fp4 v[160:161], v73, 1.0
	v_pk_fma_f32 v[120:121], v[216:217], v[152:153], v[120:121] op_sel:[1,0,0] op_sel_hi:[1,1,1]
	v_cvt_scalef32_pk_f32_fp4 v[162:163], v73, 1.0 op_sel:[1,0,0]
	v_pk_fma_f32 v[122:123], v[216:217], v[154:155], v[122:123] op_sel:[1,0,0] op_sel_hi:[1,1,1]
	v_cvt_scalef32_pk_f32_fp4 v[152:153], v73, 1.0 op_sel:[0,1,0]
	v_pk_fma_f32 v[124:125], v[216:217], v[156:157], v[124:125] op_sel:[1,0,0] op_sel_hi:[1,1,1]
	v_cvt_scalef32_pk_f32_fp4 v[154:155], v73, 1.0 op_sel:[1,1,0]
	v_pk_fma_f32 v[126:127], v[216:217], v[158:159], v[126:127] op_sel:[1,0,0] op_sel_hi:[1,1,1]
	v_cvt_scalef32_pk_f32_fp4 v[156:157], v74, 1.0
	v_pk_fma_f32 v[128:129], v[216:217], v[160:161], v[128:129] op_sel:[1,0,0] op_sel_hi:[1,1,1]
	v_cvt_scalef32_pk_f32_fp4 v[158:159], v74, 1.0 op_sel:[1,0,0]
	v_pk_fma_f32 v[130:131], v[216:217], v[162:163], v[130:131] op_sel:[1,0,0] op_sel_hi:[1,1,1]
	v_cvt_scalef32_pk_f32_fp4 v[160:161], v74, 1.0 op_sel:[0,1,0]
	v_pk_fma_f32 v[132:133], v[216:217], v[152:153], v[132:133] op_sel:[1,0,0] op_sel_hi:[1,1,1]
	v_cvt_scalef32_pk_f32_fp4 v[162:163], v74, 1.0 op_sel:[1,1,0]
	v_pk_fma_f32 v[134:135], v[216:217], v[154:155], v[134:135] op_sel:[1,0,0] op_sel_hi:[1,1,1]
	v_cvt_scalef32_pk_f32_fp4 v[152:153], v75, 1.0
	v_pk_fma_f32 v[136:137], v[216:217], v[156:157], v[136:137] op_sel:[1,0,0] op_sel_hi:[1,1,1]
	v_cvt_scalef32_pk_f32_fp4 v[154:155], v75, 1.0 op_sel:[1,0,0]
	v_pk_fma_f32 v[138:139], v[216:217], v[158:159], v[138:139] op_sel:[1,0,0] op_sel_hi:[1,1,1]
	v_cvt_scalef32_pk_f32_fp4 v[156:157], v75, 1.0 op_sel:[0,1,0]
	v_pk_fma_f32 v[140:141], v[216:217], v[160:161], v[140:141] op_sel:[1,0,0] op_sel_hi:[1,1,1]
	v_cvt_scalef32_pk_f32_fp4 v[158:159], v75, 1.0 op_sel:[1,1,0]
	v_pk_fma_f32 v[142:143], v[216:217], v[162:163], v[142:143] op_sel:[1,0,0] op_sel_hi:[1,1,1]
	v_pk_fma_f32 v[144:145], v[216:217], v[152:153], v[144:145] op_sel:[1,0,0] op_sel_hi:[1,1,1]
	v_pk_fma_f32 v[146:147], v[216:217], v[154:155], v[146:147] op_sel:[1,0,0] op_sel_hi:[1,1,1]
	v_pk_fma_f32 v[148:149], v[216:217], v[156:157], v[148:149] op_sel:[1,0,0] op_sel_hi:[1,1,1]
	v_pk_fma_f32 v[150:151], v[216:217], v[158:159], v[150:151] op_sel:[1,0,0] op_sel_hi:[1,1,1]
	s_waitcnt vmcnt(17)
	v_cvt_scalef32_pk_f32_fp4 v[152:153], v76, 1.0
	v_cvt_scalef32_pk_f32_fp4 v[154:155], v76, 1.0 op_sel:[1,0,0]
	v_cvt_scalef32_pk_f32_fp4 v[156:157], v76, 1.0 op_sel:[0,1,0]
	v_cvt_scalef32_pk_f32_fp4 v[158:159], v76, 1.0 op_sel:[1,1,0]
	v_cvt_scalef32_pk_f32_fp4 v[160:161], v77, 1.0
	v_pk_fma_f32 v[120:121], v[218:219], v[152:153], v[120:121] op_sel_hi:[0,1,1]
	v_cvt_scalef32_pk_f32_fp4 v[162:163], v77, 1.0 op_sel:[1,0,0]
	v_pk_fma_f32 v[122:123], v[218:219], v[154:155], v[122:123] op_sel_hi:[0,1,1]
	v_cvt_scalef32_pk_f32_fp4 v[152:153], v77, 1.0 op_sel:[0,1,0]
	v_pk_fma_f32 v[124:125], v[218:219], v[156:157], v[124:125] op_sel_hi:[0,1,1]
	v_cvt_scalef32_pk_f32_fp4 v[154:155], v77, 1.0 op_sel:[1,1,0]
	v_pk_fma_f32 v[126:127], v[218:219], v[158:159], v[126:127] op_sel_hi:[0,1,1]
	v_cvt_scalef32_pk_f32_fp4 v[156:157], v78, 1.0
	v_pk_fma_f32 v[128:129], v[218:219], v[160:161], v[128:129] op_sel_hi:[0,1,1]
	v_cvt_scalef32_pk_f32_fp4 v[158:159], v78, 1.0 op_sel:[1,0,0]
	v_pk_fma_f32 v[130:131], v[218:219], v[162:163], v[130:131] op_sel_hi:[0,1,1]
	v_cvt_scalef32_pk_f32_fp4 v[160:161], v78, 1.0 op_sel:[0,1,0]
	v_pk_fma_f32 v[132:133], v[218:219], v[152:153], v[132:133] op_sel_hi:[0,1,1]
	v_cvt_scalef32_pk_f32_fp4 v[162:163], v78, 1.0 op_sel:[1,1,0]
	v_pk_fma_f32 v[134:135], v[218:219], v[154:155], v[134:135] op_sel_hi:[0,1,1]
	v_cvt_scalef32_pk_f32_fp4 v[152:153], v79, 1.0
	v_pk_fma_f32 v[136:137], v[218:219], v[156:157], v[136:137] op_sel_hi:[0,1,1]
	v_cvt_scalef32_pk_f32_fp4 v[154:155], v79, 1.0 op_sel:[1,0,0]
	v_pk_fma_f32 v[138:139], v[218:219], v[158:159], v[138:139] op_sel_hi:[0,1,1]
	v_cvt_scalef32_pk_f32_fp4 v[156:157], v79, 1.0 op_sel:[0,1,0]
	v_pk_fma_f32 v[140:141], v[218:219], v[160:161], v[140:141] op_sel_hi:[0,1,1]
	v_cvt_scalef32_pk_f32_fp4 v[158:159], v79, 1.0 op_sel:[1,1,0]
	v_pk_fma_f32 v[142:143], v[218:219], v[162:163], v[142:143] op_sel_hi:[0,1,1]
	v_pk_fma_f32 v[144:145], v[218:219], v[152:153], v[144:145] op_sel_hi:[0,1,1]
	v_pk_fma_f32 v[146:147], v[218:219], v[154:155], v[146:147] op_sel_hi:[0,1,1]
	v_pk_fma_f32 v[148:149], v[218:219], v[156:157], v[148:149] op_sel_hi:[0,1,1]
	v_pk_fma_f32 v[150:151], v[218:219], v[158:159], v[150:151] op_sel_hi:[0,1,1]
	s_waitcnt vmcnt(16)
; #define EV_LOADN(q_, g0_, n_) _Pragma("unroll") for (int k = 0; k < (n_); ++k) q_[k] = __builtin_bit_cast(uint4, __builtin_amdgcn_raw_buffer_load_b128(vrs, voff + si[((g0_) + k) * 8 + sub] * 128, 0, GATHER_AUX))
; #define EV_WAIT(n_) asm volatile("s_waitcnt vmcnt(" #n_ ")" ::: "memory")
; __device__ void phase_exp_v(KParams& p, char* smem) {
;     ...
;         EV_LOADN(qa, 0, 4); EV_LOADN(qb, 4, 4); EV_LOADN(qc, 8, 4); EV_LOADN(qd, 12, 4);
;         {
;           const int t1 = (tt + 1 < 16) ? t + 1 : t;
;           e0n = p.idx[(size_t)t1 * 128 + lane]; e1n = p.idx[(size_t)t1 * 128 + 64 + lane];
;           g0n = p.gate[(size_t)t1 * 128 + lane]; g1n = p.gate[(size_t)t1 * 128 + 64 + lane];
;         }
;         EV_WAIT(16); EV_COMPN(qa, 0, 4);
;         EV_WAIT(12); EV_COMPN(qb, 4, 4);
;         EV_WAIT(8); EV_COMPN(qc, 8, 4);
;         EV_WAIT(4); EV_COMPN(qd, 12, 4);
	v_cvt_scalef32_pk_f32_fp4 v[152:153], v80, 1.0
	v_cvt_scalef32_pk_f32_fp4 v[154:155], v80, 1.0 op_sel:[1,0,0]
	v_cvt_scalef32_pk_f32_fp4 v[156:157], v80, 1.0 op_sel:[0,1,0]
	v_cvt_scalef32_pk_f32_fp4 v[158:159], v80, 1.0 op_sel:[1,1,0]
	v_cvt_scalef32_pk_f32_fp4 v[160:161], v81, 1.0
	v_pk_fma_f32 v[120:121], v[218:219], v[152:153], v[120:121] op_sel:[1,0,0] op_sel_hi:[1,1,1]
	v_cvt_scalef32_pk_f32_fp4 v[162:163], v81, 1.0 op_sel:[1,0,0]
	v_pk_fma_f32 v[122:123], v[218:219], v[154:155], v[122:123] op_sel:[1,0,0] op_sel_hi:[1,1,1]
	v_cvt_scalef32_pk_f32_fp4 v[152:153], v81, 1.0 op_sel:[0,1,0]
	v_pk_fma_f32 v[124:125], v[218:219], v[156:157], v[124:125] op_sel:[1,0,0] op_sel_hi:[1,1,1]
	v_cvt_scalef32_pk_f32_fp4 v[154:155], v81, 1.0 op_sel:[1,1,0]
	v_pk_fma_f32 v[126:127], v[218:219], v[158:159], v[126:127] op_sel:[1,0,0] op_sel_hi:[1,1,1]
	v_cvt_scalef32_pk_f32_fp4 v[156:157], v82, 1.0
	v_pk_fma_f32 v[128:129], v[218:219], v[160:161], v[128:129] op_sel:[1,0,0] op_sel_hi:[1,1,1]
	v_cvt_scalef32_pk_f32_fp4 v[158:159], v82, 1.0 op_sel:[1,0,0]
	v_pk_fma_f32 v[130:131], v[218:219], v[162:163], v[130:131] op_sel:[1,0,0] op_sel_hi:[1,1,1]
	v_cvt_scalef32_pk_f32_fp4 v[160:161], v82, 1.0 op_sel:[0,1,0]
	v_pk_fma_f32 v[132:133], v[218:219], v[152:153], v[132:133] op_sel:[1,0,0] op_sel_hi:[1,1,1]
	v_cvt_scalef32_pk_f32_fp4 v[162:163], v82, 1.0 op_sel:[1,1,0]
	v_pk_fma_f32 v[134:135], v[218:219], v[154:155], v[134:135] op_sel:[1,0,0] op_sel_hi:[1,1,1]
	v_cvt_scalef32_pk_f32_fp4 v[152:153], v83, 1.0
	v_pk_fma_f32 v[136:137], v[218:219], v[156:157], v[136:137] op_sel:[1,0,0] op_sel_hi:[1,1,1]
	v_cvt_scalef32_pk_f32_fp4 v[154:155], v83, 1.0 op_sel:[1,0,0]
	v_pk_fma_f32 v[138:139], v[218:219], v[158:159], v[138:139] op_sel:[1,0,0] op_sel_hi:[1,1,1]
	v_cvt_scalef32_pk_f32_fp4 v[156:157], v83, 1.0 op_sel:[0,1,0]
	v_pk_fma_f32 v[140:141], v[218:219], v[160:161], v[140:141] op_sel:[1,0,0] op_sel_hi:[1,1,1]
	v_cvt_scalef32_pk_f32_fp4 v[158:159], v83, 1.0 op_sel:[1,1,0]
	v_pk_fma_f32 v[142:143], v[218:219], v[162:163], v[142:143] op_sel:[1,0,0] op_sel_hi:[1,1,1]
	v_pk_fma_f32 v[144:145], v[218:219], v[152:153], v[144:145] op_sel:[1,0,0] op_sel_hi:[1,1,1]
	v_pk_fma_f32 v[146:147], v[218:219], v[154:155], v[146:147] op_sel:[1,0,0] op_sel_hi:[1,1,1]
	v_pk_fma_f32 v[148:149], v[218:219], v[156:157], v[148:149] op_sel:[1,0,0] op_sel_hi:[1,1,1]
	v_pk_fma_f32 v[150:151], v[218:219], v[158:159], v[150:151] op_sel:[1,0,0] op_sel_hi:[1,1,1]
	s_waitcnt vmcnt(15)
	v_cvt_scalef32_pk_f32_fp4 v[152:153], v84, 1.0
	v_cvt_scalef32_pk_f32_fp4 v[154:155], v84, 1.0 op_sel:[1,0,0]
	v_cvt_scalef32_pk_f32_fp4 v[156:157], v84, 1.0 op_sel:[0,1,0]
	v_cvt_scalef32_pk_f32_fp4 v[158:159], v84, 1.0 op_sel:[1,1,0]
	v_cvt_scalef32_pk_f32_fp4 v[160:161], v85, 1.0
	v_pk_fma_f32 v[120:121], v[220:221], v[152:153], v[120:121] op_sel_hi:[0,1,1]
	v_cvt_scalef32_pk_f32_fp4 v[162:163], v85, 1.0 op_sel:[1,0,0]
	v_pk_fma_f32 v[122:123], v[220:221], v[154:155], v[122:123] op_sel_hi:[0,1,1]
	v_cvt_scalef32_pk_f32_fp4 v[152:153], v85, 1.0 op_sel:[0,1,0]
	v_pk_fma_f32 v[124:125], v[220:221], v[156:157], v[124:125] op_sel_hi:[0,1,1]
	v_cvt_scalef32_pk_f32_fp4 v[154:155], v85, 1.0 op_sel:[1,1,0]
	v_pk_fma_f32 v[126:127], v[220:221], v[158:159], v[126:127] op_sel_hi:[0,1,1]
	v_cvt_scalef32_pk_f32_fp4 v[156:157], v86, 1.0
	v_pk_fma_f32 v[128:129], v[220:221], v[160:161], v[128:129] op_sel_hi:[0,1,1]
	v_cvt_scalef32_pk_f32_fp4 v[158:159], v86, 1.0 op_sel:[1,0,0]
	v_pk_fma_f32 v[130:131], v[220:221], v[162:163], v[130:131] op_sel_hi:[0,1,1]
	v_cvt_scalef32_pk_f32_fp4 v[160:161], v86, 1.0 op_sel:[0,1,0]
	v_pk_fma_f32 v[132:133], v[220:221], v[152:153], v[132:133] op_sel_hi:[0,1,1]
	v_cvt_scalef32_pk_f32_fp4 v[162:163], v86, 1.0 op_sel:[1,1,0]
	v_pk_fma_f32 v[134:135], v[220:221], v[154:155], v[134:135] op_sel_hi:[0,1,1]
	v_cvt_scalef32_pk_f32_fp4 v[152:153], v87, 1.0
	v_pk_fma_f32 v[136:137], v[220:221], v[156:157], v[136:137] op_sel_hi:[0,1,1]
	v_cvt_scalef32_pk_f32_fp4 v[154:155], v87, 1.0 op_sel:[1,0,0]
	v_pk_fma_f32 v[138:139], v[220:221], v[158:159], v[138:139] op_sel_hi:[0,1,1]
	v_cvt_scalef32_pk_f32_fp4 v[156:157], v87, 1.0 op_sel:[0,1,0]
	v_pk_fma_f32 v[140:141], v[220:221], v[160:161], v[140:141] op_sel_hi:[0,1,1]
	v_cvt_scalef32_pk_f32_fp4 v[158:159], v87, 1.0 op_sel:[1,1,0]
	v_pk_fma_f32 v[142:143], v[220:221], v[162:163], v[142:143] op_sel_hi:[0,1,1]
	v_pk_fma_f32 v[144:145], v[220:221], v[152:153], v[144:145] op_sel_hi:[0,1,1]
	v_pk_fma_f32 v[146:147], v[220:221], v[154:155], v[146:147] op_sel_hi:[0,1,1]
	v_pk_fma_f32 v[148:149], v[220:221], v[156:157], v[148:149] op_sel_hi:[0,1,1]
	v_pk_fma_f32 v[150:151], v[220:221], v[158:159], v[150:151] op_sel_hi:[0,1,1]
	s_waitcnt vmcnt(14)
; #define EV_LOADN(q_, g0_, n_) _Pragma("unroll") for (int k = 0; k < (n_); ++k) q_[k] = __builtin_bit_cast(uint4, __builtin_amdgcn_raw_buffer_load_b128(vrs, voff + si[((g0_) + k) * 8 + sub] * 128, 0, GATHER_AUX))
; #define EV_WAIT(n_) asm volatile("s_waitcnt vmcnt(" #n_ ")" ::: "memory")
; __device__ void phase_exp_v(KParams& p, char* smem) {
;     ...
;         EV_LOADN(qa, 0, 4); EV_LOADN(qb, 4, 4); EV_LOADN(qc, 8, 4); EV_LOADN(qd, 12, 4);
;         {
;           const int t1 = (tt + 1 < 16) ? t + 1 : t;
;           e0n = p.idx[(size_t)t1 * 128 + lane]; e1n = p.idx[(size_t)t1 * 128 + 64 + lane];
;           g0n = p.gate[(size_t)t1 * 128 + lane]; g1n = p.gate[(size_t)t1 * 128 + 64 + lane];
;         }
;         EV_WAIT(16); EV_COMPN(qa, 0, 4);
;         EV_WAIT(12); EV_COMPN(qb, 4, 4);
;         EV_WAIT(8); EV_COMPN(qc, 8, 4);
;         EV_WAIT(4); EV_COMPN(qd, 12, 4);
	v_cvt_scalef32_pk_f32_fp4 v[152:153], v40, 1.0
	v_cvt_scalef32_pk_f32_fp4 v[154:155], v40, 1.0 op_sel:[1,0,0]
	v_cvt_scalef32_pk_f32_fp4 v[156:157], v40, 1.0 op_sel:[0,1,0]
	v_cvt_scalef32_pk_f32_fp4 v[158:159], v40, 1.0 op_sel:[1,1,0]
	v_cvt_scalef32_pk_f32_fp4 v[160:161], v41, 1.0
	v_pk_fma_f32 v[120:121], v[220:221], v[152:153], v[120:121] op_sel:[1,0,0] op_sel_hi:[1,1,1]
	v_cvt_scalef32_pk_f32_fp4 v[162:163], v41, 1.0 op_sel:[1,0,0]
	v_pk_fma_f32 v[122:123], v[220:221], v[154:155], v[122:123] op_sel:[1,0,0] op_sel_hi:[1,1,1]
	v_cvt_scalef32_pk_f32_fp4 v[152:153], v41, 1.0 op_sel:[0,1,0]
	v_pk_fma_f32 v[124:125], v[220:221], v[156:157], v[124:125] op_sel:[1,0,0] op_sel_hi:[1,1,1]
	v_cvt_scalef32_pk_f32_fp4 v[154:155], v41, 1.0 op_sel:[1,1,0]
	v_pk_fma_f32 v[126:127], v[220:221], v[158:159], v[126:127] op_sel:[1,0,0] op_sel_hi:[1,1,1]
	v_cvt_scalef32_pk_f32_fp4 v[156:157], v42, 1.0
	v_pk_fma_f32 v[128:129], v[220:221], v[160:161], v[128:129] op_sel:[1,0,0] op_sel_hi:[1,1,1]
	v_cvt_scalef32_pk_f32_fp4 v[158:159], v42, 1.0 op_sel:[1,0,0]
	v_pk_fma_f32 v[130:131], v[220:221], v[162:163], v[130:131] op_sel:[1,0,0] op_sel_hi:[1,1,1]
	v_cvt_scalef32_pk_f32_fp4 v[160:161], v42, 1.0 op_sel:[0,1,0]
	v_pk_fma_f32 v[132:133], v[220:221], v[152:153], v[132:133] op_sel:[1,0,0] op_sel_hi:[1,1,1]
	v_cvt_scalef32_pk_f32_fp4 v[162:163], v42, 1.0 op_sel:[1,1,0]
	v_pk_fma_f32 v[134:135], v[220:221], v[154:155], v[134:135] op_sel:[1,0,0] op_sel_hi:[1,1,1]
	v_cvt_scalef32_pk_f32_fp4 v[152:153], v43, 1.0
	v_pk_fma_f32 v[136:137], v[220:221], v[156:157], v[136:137] op_sel:[1,0,0] op_sel_hi:[1,1,1]
	v_cvt_scalef32_pk_f32_fp4 v[154:155], v43, 1.0 op_sel:[1,0,0]
	v_pk_fma_f32 v[138:139], v[220:221], v[158:159], v[138:139] op_sel:[1,0,0] op_sel_hi:[1,1,1]
	v_cvt_scalef32_pk_f32_fp4 v[156:157], v43, 1.0 op_sel:[0,1,0]
	v_pk_fma_f32 v[140:141], v[220:221], v[160:161], v[140:141] op_sel:[1,0,0] op_sel_hi:[1,1,1]
	v_cvt_scalef32_pk_f32_fp4 v[158:159], v43, 1.0 op_sel:[1,1,0]
	v_pk_fma_f32 v[142:143], v[220:221], v[162:163], v[142:143] op_sel:[1,0,0] op_sel_hi:[1,1,1]
	v_pk_fma_f32 v[144:145], v[220:221], v[152:153], v[144:145] op_sel:[1,0,0] op_sel_hi:[1,1,1]
	v_pk_fma_f32 v[146:147], v[220:221], v[154:155], v[146:147] op_sel:[1,0,0] op_sel_hi:[1,1,1]
	v_pk_fma_f32 v[148:149], v[220:221], v[156:157], v[148:149] op_sel:[1,0,0] op_sel_hi:[1,1,1]
	v_pk_fma_f32 v[150:151], v[220:221], v[158:159], v[150:151] op_sel:[1,0,0] op_sel_hi:[1,1,1]
	s_waitcnt vmcnt(13)
	v_cvt_scalef32_pk_f32_fp4 v[152:153], v36, 1.0
	v_cvt_scalef32_pk_f32_fp4 v[154:155], v36, 1.0 op_sel:[1,0,0]
	v_cvt_scalef32_pk_f32_fp4 v[156:157], v36, 1.0 op_sel:[0,1,0]
	v_cvt_scalef32_pk_f32_fp4 v[158:159], v36, 1.0 op_sel:[1,1,0]
	v_cvt_scalef32_pk_f32_fp4 v[160:161], v37, 1.0
	v_pk_fma_f32 v[120:121], v[222:223], v[152:153], v[120:121] op_sel_hi:[0,1,1]
	v_cvt_scalef32_pk_f32_fp4 v[162:163], v37, 1.0 op_sel:[1,0,0]
	v_pk_fma_f32 v[122:123], v[222:223], v[154:155], v[122:123] op_sel_hi:[0,1,1]
	v_cvt_scalef32_pk_f32_fp4 v[152:153], v37, 1.0 op_sel:[0,1,0]
	v_pk_fma_f32 v[124:125], v[222:223], v[156:157], v[124:125] op_sel_hi:[0,1,1]
	v_cvt_scalef32_pk_f32_fp4 v[154:155], v37, 1.0 op_sel:[1,1,0]
	v_pk_fma_f32 v[126:127], v[222:223], v[158:159], v[126:127] op_sel_hi:[0,1,1]
	v_cvt_scalef32_pk_f32_fp4 v[156:157], v38, 1.0
	v_pk_fma_f32 v[128:129], v[222:223], v[160:161], v[128:129] op_sel_hi:[0,1,1]
	v_cvt_scalef32_pk_f32_fp4 v[158:159], v38, 1.0 op_sel:[1,0,0]
	v_pk_fma_f32 v[130:131], v[222:223], v[162:163], v[130:131] op_sel_hi:[0,1,1]
	v_cvt_scalef32_pk_f32_fp4 v[160:161], v38, 1.0 op_sel:[0,1,0]
	v_pk_fma_f32 v[132:133], v[222:223], v[152:153], v[132:133] op_sel_hi:[0,1,1]
	v_cvt_scalef32_pk_f32_fp4 v[162:163], v38, 1.0 op_sel:[1,1,0]
	v_pk_fma_f32 v[134:135], v[222:223], v[154:155], v[134:135] op_sel_hi:[0,1,1]
	v_cvt_scalef32_pk_f32_fp4 v[152:153], v39, 1.0
	v_pk_fma_f32 v[136:137], v[222:223], v[156:157], v[136:137] op_sel_hi:[0,1,1]
	v_cvt_scalef32_pk_f32_fp4 v[154:155], v39, 1.0 op_sel:[1,0,0]
	v_pk_fma_f32 v[138:139], v[222:223], v[158:159], v[138:139] op_sel_hi:[0,1,1]
	v_cvt_scalef32_pk_f32_fp4 v[156:157], v39, 1.0 op_sel:[0,1,0]
	v_pk_fma_f32 v[140:141], v[222:223], v[160:161], v[140:141] op_sel_hi:[0,1,1]
	v_cvt_scalef32_pk_f32_fp4 v[158:159], v39, 1.0 op_sel:[1,1,0]
	v_pk_fma_f32 v[142:143], v[222:223], v[162:163], v[142:143] op_sel_hi:[0,1,1]
	v_pk_fma_f32 v[144:145], v[222:223], v[152:153], v[144:145] op_sel_hi:[0,1,1]
	v_pk_fma_f32 v[146:147], v[222:223], v[154:155], v[146:147] op_sel_hi:[0,1,1]
	v_pk_fma_f32 v[148:149], v[222:223], v[156:157], v[148:149] op_sel_hi:[0,1,1]
	v_pk_fma_f32 v[150:151], v[222:223], v[158:159], v[150:151] op_sel_hi:[0,1,1]
	s_waitcnt vmcnt(12)
; #define EV_LOADN(q_, g0_, n_) _Pragma("unroll") for (int k = 0; k < (n_); ++k) q_[k] = __builtin_bit_cast(uint4, __builtin_amdgcn_raw_buffer_load_b128(vrs, voff + si[((g0_) + k) * 8 + sub] * 128, 0, GATHER_AUX))
; #define EV_WAIT(n_) asm volatile("s_waitcnt vmcnt(" #n_ ")" ::: "memory")
; __device__ void phase_exp_v(KParams& p, char* smem) {
;     ...
;         EV_LOADN(qa, 0, 4); EV_LOADN(qb, 4, 4); EV_LOADN(qc, 8, 4); EV_LOADN(qd, 12, 4);
;         {
;           const int t1 = (tt + 1 < 16) ? t + 1 : t;
;           e0n = p.idx[(size_t)t1 * 128 + lane]; e1n = p.idx[(size_t)t1 * 128 + 64 + lane];
;           g0n = p.gate[(size_t)t1 * 128 + lane]; g1n = p.gate[(size_t)t1 * 128 + 64 + lane];
;         }
;         EV_WAIT(16); EV_COMPN(qa, 0, 4);
;         EV_WAIT(12); EV_COMPN(qb, 4, 4);
;         EV_WAIT(8); EV_COMPN(qc, 8, 4);
;         EV_WAIT(4); EV_COMPN(qd, 12, 4);
	v_cvt_scalef32_pk_f32_fp4 v[152:153], v32, 1.0
	v_cvt_scalef32_pk_f32_fp4 v[154:155], v32, 1.0 op_sel:[1,0,0]
	v_cvt_scalef32_pk_f32_fp4 v[156:157], v32, 1.0 op_sel:[0,1,0]
	v_cvt_scalef32_pk_f32_fp4 v[158:159], v32, 1.0 op_sel:[1,1,0]
	v_cvt_scalef32_pk_f32_fp4 v[160:161], v33, 1.0
	v_pk_fma_f32 v[120:121], v[222:223], v[152:153], v[120:121] op_sel:[1,0,0] op_sel_hi:[1,1,1]
	v_cvt_scalef32_pk_f32_fp4 v[162:163], v33, 1.0 op_sel:[1,0,0]
	v_pk_fma_f32 v[122:123], v[222:223], v[154:155], v[122:123] op_sel:[1,0,0] op_sel_hi:[1,1,1]
	v_cvt_scalef32_pk_f32_fp4 v[152:153], v33, 1.0 op_sel:[0,1,0]
	v_pk_fma_f32 v[124:125], v[222:223], v[156:157], v[124:125] op_sel:[1,0,0] op_sel_hi:[1,1,1]
	v_cvt_scalef32_pk_f32_fp4 v[154:155], v33, 1.0 op_sel:[1,1,0]
	v_pk_fma_f32 v[126:127], v[222:223], v[158:159], v[126:127] op_sel:[1,0,0] op_sel_hi:[1,1,1]
	v_cvt_scalef32_pk_f32_fp4 v[156:157], v34, 1.0
	v_pk_fma_f32 v[128:129], v[222:223], v[160:161], v[128:129] op_sel:[1,0,0] op_sel_hi:[1,1,1]
	v_cvt_scalef32_pk_f32_fp4 v[158:159], v34, 1.0 op_sel:[1,0,0]
	v_pk_fma_f32 v[130:131], v[222:223], v[162:163], v[130:131] op_sel:[1,0,0] op_sel_hi:[1,1,1]
	v_cvt_scalef32_pk_f32_fp4 v[160:161], v34, 1.0 op_sel:[0,1,0]
	v_pk_fma_f32 v[132:133], v[222:223], v[152:153], v[132:133] op_sel:[1,0,0] op_sel_hi:[1,1,1]
	v_cvt_scalef32_pk_f32_fp4 v[162:163], v34, 1.0 op_sel:[1,1,0]
	v_pk_fma_f32 v[134:135], v[222:223], v[154:155], v[134:135] op_sel:[1,0,0] op_sel_hi:[1,1,1]
	v_cvt_scalef32_pk_f32_fp4 v[152:153], v35, 1.0
	v_pk_fma_f32 v[136:137], v[222:223], v[156:157], v[136:137] op_sel:[1,0,0] op_sel_hi:[1,1,1]
	v_cvt_scalef32_pk_f32_fp4 v[154:155], v35, 1.0 op_sel:[1,0,0]
	v_pk_fma_f32 v[138:139], v[222:223], v[158:159], v[138:139] op_sel:[1,0,0] op_sel_hi:[1,1,1]
	v_cvt_scalef32_pk_f32_fp4 v[156:157], v35, 1.0 op_sel:[0,1,0]
	v_pk_fma_f32 v[140:141], v[222:223], v[160:161], v[140:141] op_sel:[1,0,0] op_sel_hi:[1,1,1]
	v_cvt_scalef32_pk_f32_fp4 v[158:159], v35, 1.0 op_sel:[1,1,0]
	v_pk_fma_f32 v[142:143], v[222:223], v[162:163], v[142:143] op_sel:[1,0,0] op_sel_hi:[1,1,1]
	v_pk_fma_f32 v[144:145], v[222:223], v[152:153], v[144:145] op_sel:[1,0,0] op_sel_hi:[1,1,1]
	v_pk_fma_f32 v[146:147], v[222:223], v[154:155], v[146:147] op_sel:[1,0,0] op_sel_hi:[1,1,1]
	v_pk_fma_f32 v[148:149], v[222:223], v[156:157], v[148:149] op_sel:[1,0,0] op_sel_hi:[1,1,1]
	v_pk_fma_f32 v[150:151], v[222:223], v[158:159], v[150:151] op_sel:[1,0,0] op_sel_hi:[1,1,1]
	s_waitcnt vmcnt(11)
	v_cvt_scalef32_pk_f32_fp4 v[152:153], v28, 1.0
	v_cvt_scalef32_pk_f32_fp4 v[154:155], v28, 1.0 op_sel:[1,0,0]
	v_cvt_scalef32_pk_f32_fp4 v[156:157], v28, 1.0 op_sel:[0,1,0]
	v_cvt_scalef32_pk_f32_fp4 v[158:159], v28, 1.0 op_sel:[1,1,0]
	v_cvt_scalef32_pk_f32_fp4 v[160:161], v29, 1.0
	v_pk_fma_f32 v[120:121], v[224:225], v[152:153], v[120:121] op_sel_hi:[0,1,1]
	v_cvt_scalef32_pk_f32_fp4 v[162:163], v29, 1.0 op_sel:[1,0,0]
	v_pk_fma_f32 v[122:123], v[224:225], v[154:155], v[122:123] op_sel_hi:[0,1,1]
	v_cvt_scalef32_pk_f32_fp4 v[152:153], v29, 1.0 op_sel:[0,1,0]
	v_pk_fma_f32 v[124:125], v[224:225], v[156:157], v[124:125] op_sel_hi:[0,1,1]
	v_cvt_scalef32_pk_f32_fp4 v[154:155], v29, 1.0 op_sel:[1,1,0]
	v_pk_fma_f32 v[126:127], v[224:225], v[158:159], v[126:127] op_sel_hi:[0,1,1]
	v_cvt_scalef32_pk_f32_fp4 v[156:157], v30, 1.0
	v_pk_fma_f32 v[128:129], v[224:225], v[160:161], v[128:129] op_sel_hi:[0,1,1]
	v_cvt_scalef32_pk_f32_fp4 v[158:159], v30, 1.0 op_sel:[1,0,0]
	v_pk_fma_f32 v[130:131], v[224:225], v[162:163], v[130:131] op_sel_hi:[0,1,1]
	v_cvt_scalef32_pk_f32_fp4 v[160:161], v30, 1.0 op_sel:[0,1,0]
	v_pk_fma_f32 v[132:133], v[224:225], v[152:153], v[132:133] op_sel_hi:[0,1,1]
	v_cvt_scalef32_pk_f32_fp4 v[162:163], v30, 1.0 op_sel:[1,1,0]
	v_pk_fma_f32 v[134:135], v[224:225], v[154:155], v[134:135] op_sel_hi:[0,1,1]
	v_cvt_scalef32_pk_f32_fp4 v[152:153], v31, 1.0
	v_pk_fma_f32 v[136:137], v[224:225], v[156:157], v[136:137] op_sel_hi:[0,1,1]
	v_cvt_scalef32_pk_f32_fp4 v[154:155], v31, 1.0 op_sel:[1,0,0]
	v_pk_fma_f32 v[138:139], v[224:225], v[158:159], v[138:139] op_sel_hi:[0,1,1]
	v_cvt_scalef32_pk_f32_fp4 v[156:157], v31, 1.0 op_sel:[0,1,0]
	v_pk_fma_f32 v[140:141], v[224:225], v[160:161], v[140:141] op_sel_hi:[0,1,1]
	v_cvt_scalef32_pk_f32_fp4 v[158:159], v31, 1.0 op_sel:[1,1,0]
	v_pk_fma_f32 v[142:143], v[224:225], v[162:163], v[142:143] op_sel_hi:[0,1,1]
	v_pk_fma_f32 v[144:145], v[224:225], v[152:153], v[144:145] op_sel_hi:[0,1,1]
	v_pk_fma_f32 v[146:147], v[224:225], v[154:155], v[146:147] op_sel_hi:[0,1,1]
	v_pk_fma_f32 v[148:149], v[224:225], v[156:157], v[148:149] op_sel_hi:[0,1,1]
	v_pk_fma_f32 v[150:151], v[224:225], v[158:159], v[150:151] op_sel_hi:[0,1,1]
	s_waitcnt vmcnt(10)
; #define EV_LOADN(q_, g0_, n_) _Pragma("unroll") for (int k = 0; k < (n_); ++k) q_[k] = __builtin_bit_cast(uint4, __builtin_amdgcn_raw_buffer_load_b128(vrs, voff + si[((g0_) + k) * 8 + sub] * 128, 0, GATHER_AUX))
; #define EV_WAIT(n_) asm volatile("s_waitcnt vmcnt(" #n_ ")" ::: "memory")
; __device__ void phase_exp_v(KParams& p, char* smem) {
;     ...
;         EV_LOADN(qa, 0, 4); EV_LOADN(qb, 4, 4); EV_LOADN(qc, 8, 4); EV_LOADN(qd, 12, 4);
;         {
;           const int t1 = (tt + 1 < 16) ? t + 1 : t;
;           e0n = p.idx[(size_t)t1 * 128 + lane]; e1n = p.idx[(size_t)t1 * 128 + 64 + lane];
;           g0n = p.gate[(size_t)t1 * 128 + lane]; g1n = p.gate[(size_t)t1 * 128 + 64 + lane];
;         }
;         EV_WAIT(16); EV_COMPN(qa, 0, 4);
;         EV_WAIT(12); EV_COMPN(qb, 4, 4);
;         EV_WAIT(8); EV_COMPN(qc, 8, 4);
;         EV_WAIT(4); EV_COMPN(qd, 12, 4);
	v_cvt_scalef32_pk_f32_fp4 v[152:153], v24, 1.0
	v_cvt_scalef32_pk_f32_fp4 v[154:155], v24, 1.0 op_sel:[1,0,0]
	v_cvt_scalef32_pk_f32_fp4 v[156:157], v24, 1.0 op_sel:[0,1,0]
	v_cvt_scalef32_pk_f32_fp4 v[158:159], v24, 1.0 op_sel:[1,1,0]
	v_cvt_scalef32_pk_f32_fp4 v[160:161], v25, 1.0
	v_pk_fma_f32 v[120:121], v[224:225], v[152:153], v[120:121] op_sel:[1,0,0] op_sel_hi:[1,1,1]
	v_cvt_scalef32_pk_f32_fp4 v[162:163], v25, 1.0 op_sel:[1,0,0]
	v_pk_fma_f32 v[122:123], v[224:225], v[154:155], v[122:123] op_sel:[1,0,0] op_sel_hi:[1,1,1]
	v_cvt_scalef32_pk_f32_fp4 v[152:153], v25, 1.0 op_sel:[0,1,0]
	v_pk_fma_f32 v[124:125], v[224:225], v[156:157], v[124:125] op_sel:[1,0,0] op_sel_hi:[1,1,1]
	v_cvt_scalef32_pk_f32_fp4 v[154:155], v25, 1.0 op_sel:[1,1,0]
	v_pk_fma_f32 v[126:127], v[224:225], v[158:159], v[126:127] op_sel:[1,0,0] op_sel_hi:[1,1,1]
	v_cvt_scalef32_pk_f32_fp4 v[156:157], v26, 1.0
	v_pk_fma_f32 v[128:129], v[224:225], v[160:161], v[128:129] op_sel:[1,0,0] op_sel_hi:[1,1,1]
	v_cvt_scalef32_pk_f32_fp4 v[158:159], v26, 1.0 op_sel:[1,0,0]
	v_pk_fma_f32 v[130:131], v[224:225], v[162:163], v[130:131] op_sel:[1,0,0] op_sel_hi:[1,1,1]
	v_cvt_scalef32_pk_f32_fp4 v[160:161], v26, 1.0 op_sel:[0,1,0]
	v_pk_fma_f32 v[132:133], v[224:225], v[152:153], v[132:133] op_sel:[1,0,0] op_sel_hi:[1,1,1]
	v_cvt_scalef32_pk_f32_fp4 v[162:163], v26, 1.0 op_sel:[1,1,0]
	v_pk_fma_f32 v[134:135], v[224:225], v[154:155], v[134:135] op_sel:[1,0,0] op_sel_hi:[1,1,1]
	v_cvt_scalef32_pk_f32_fp4 v[152:153], v27, 1.0
	v_pk_fma_f32 v[136:137], v[224:225], v[156:157], v[136:137] op_sel:[1,0,0] op_sel_hi:[1,1,1]
	v_cvt_scalef32_pk_f32_fp4 v[154:155], v27, 1.0 op_sel:[1,0,0]
	v_pk_fma_f32 v[138:139], v[224:225], v[158:159], v[138:139] op_sel:[1,0,0] op_sel_hi:[1,1,1]
	v_cvt_scalef32_pk_f32_fp4 v[156:157], v27, 1.0 op_sel:[0,1,0]
	v_pk_fma_f32 v[140:141], v[224:225], v[160:161], v[140:141] op_sel:[1,0,0] op_sel_hi:[1,1,1]
	v_cvt_scalef32_pk_f32_fp4 v[158:159], v27, 1.0 op_sel:[1,1,0]
	v_pk_fma_f32 v[142:143], v[224:225], v[162:163], v[142:143] op_sel:[1,0,0] op_sel_hi:[1,1,1]
	v_pk_fma_f32 v[144:145], v[224:225], v[152:153], v[144:145] op_sel:[1,0,0] op_sel_hi:[1,1,1]
	v_pk_fma_f32 v[146:147], v[224:225], v[154:155], v[146:147] op_sel:[1,0,0] op_sel_hi:[1,1,1]
	v_pk_fma_f32 v[148:149], v[224:225], v[156:157], v[148:149] op_sel:[1,0,0] op_sel_hi:[1,1,1]
	v_pk_fma_f32 v[150:151], v[224:225], v[158:159], v[150:151] op_sel:[1,0,0] op_sel_hi:[1,1,1]
	s_waitcnt vmcnt(9)
	v_cvt_scalef32_pk_f32_fp4 v[152:153], v20, 1.0
	v_cvt_scalef32_pk_f32_fp4 v[154:155], v20, 1.0 op_sel:[1,0,0]
	v_cvt_scalef32_pk_f32_fp4 v[156:157], v20, 1.0 op_sel:[0,1,0]
	v_cvt_scalef32_pk_f32_fp4 v[158:159], v20, 1.0 op_sel:[1,1,0]
	v_cvt_scalef32_pk_f32_fp4 v[160:161], v21, 1.0
	v_pk_fma_f32 v[120:121], v[226:227], v[152:153], v[120:121] op_sel_hi:[0,1,1]
	v_cvt_scalef32_pk_f32_fp4 v[162:163], v21, 1.0 op_sel:[1,0,0]
	v_pk_fma_f32 v[122:123], v[226:227], v[154:155], v[122:123] op_sel_hi:[0,1,1]
	v_cvt_scalef32_pk_f32_fp4 v[152:153], v21, 1.0 op_sel:[0,1,0]
	v_pk_fma_f32 v[124:125], v[226:227], v[156:157], v[124:125] op_sel_hi:[0,1,1]
	v_cvt_scalef32_pk_f32_fp4 v[154:155], v21, 1.0 op_sel:[1,1,0]
	v_pk_fma_f32 v[126:127], v[226:227], v[158:159], v[126:127] op_sel_hi:[0,1,1]
	v_cvt_scalef32_pk_f32_fp4 v[156:157], v22, 1.0
	v_pk_fma_f32 v[128:129], v[226:227], v[160:161], v[128:129] op_sel_hi:[0,1,1]
	v_cvt_scalef32_pk_f32_fp4 v[158:159], v22, 1.0 op_sel:[1,0,0]
	v_pk_fma_f32 v[130:131], v[226:227], v[162:163], v[130:131] op_sel_hi:[0,1,1]
	v_cvt_scalef32_pk_f32_fp4 v[160:161], v22, 1.0 op_sel:[0,1,0]
	v_pk_fma_f32 v[132:133], v[226:227], v[152:153], v[132:133] op_sel_hi:[0,1,1]
	v_cvt_scalef32_pk_f32_fp4 v[162:163], v22, 1.0 op_sel:[1,1,0]
	v_pk_fma_f32 v[134:135], v[226:227], v[154:155], v[134:135] op_sel_hi:[0,1,1]
	v_cvt_scalef32_pk_f32_fp4 v[152:153], v23, 1.0
	v_pk_fma_f32 v[136:137], v[226:227], v[156:157], v[136:137] op_sel_hi:[0,1,1]
	v_cvt_scalef32_pk_f32_fp4 v[154:155], v23, 1.0 op_sel:[1,0,0]
	v_pk_fma_f32 v[138:139], v[226:227], v[158:159], v[138:139] op_sel_hi:[0,1,1]
	v_cvt_scalef32_pk_f32_fp4 v[156:157], v23, 1.0 op_sel:[0,1,0]
	v_pk_fma_f32 v[140:141], v[226:227], v[160:161], v[140:141] op_sel_hi:[0,1,1]
	v_cvt_scalef32_pk_f32_fp4 v[158:159], v23, 1.0 op_sel:[1,1,0]
	v_pk_fma_f32 v[142:143], v[226:227], v[162:163], v[142:143] op_sel_hi:[0,1,1]
	v_pk_fma_f32 v[144:145], v[226:227], v[152:153], v[144:145] op_sel_hi:[0,1,1]
	v_pk_fma_f32 v[146:147], v[226:227], v[154:155], v[146:147] op_sel_hi:[0,1,1]
	v_pk_fma_f32 v[148:149], v[226:227], v[156:157], v[148:149] op_sel_hi:[0,1,1]
	v_pk_fma_f32 v[150:151], v[226:227], v[158:159], v[150:151] op_sel_hi:[0,1,1]
	s_waitcnt vmcnt(8)
; #define EV_LOADN(q_, g0_, n_) _Pragma("unroll") for (int k = 0; k < (n_); ++k) q_[k] = __builtin_bit_cast(uint4, __builtin_amdgcn_raw_buffer_load_b128(vrs, voff + si[((g0_) + k) * 8 + sub] * 128, 0, GATHER_AUX))
; #define EV_WAIT(n_) asm volatile("s_waitcnt vmcnt(" #n_ ")" ::: "memory")
; __device__ void phase_exp_v(KParams& p, char* smem) {
;     ...
;         EV_LOADN(qa, 0, 4); EV_LOADN(qb, 4, 4); EV_LOADN(qc, 8, 4); EV_LOADN(qd, 12, 4);
;         {
;           const int t1 = (tt + 1 < 16) ? t + 1 : t;
;           e0n = p.idx[(size_t)t1 * 128 + lane]; e1n = p.idx[(size_t)t1 * 128 + 64 + lane];
;           g0n = p.gate[(size_t)t1 * 128 + lane]; g1n = p.gate[(size_t)t1 * 128 + 64 + lane];
;         }
;         EV_WAIT(16); EV_COMPN(qa, 0, 4);
;         EV_WAIT(12); EV_COMPN(qb, 4, 4);
;         EV_WAIT(8); EV_COMPN(qc, 8, 4);
;         EV_WAIT(4); EV_COMPN(qd, 12, 4);
	v_cvt_scalef32_pk_f32_fp4 v[152:153], v16, 1.0
	v_cvt_scalef32_pk_f32_fp4 v[154:155], v16, 1.0 op_sel:[1,0,0]
	v_cvt_scalef32_pk_f32_fp4 v[156:157], v16, 1.0 op_sel:[0,1,0]
	v_cvt_scalef32_pk_f32_fp4 v[158:159], v16, 1.0 op_sel:[1,1,0]
	v_cvt_scalef32_pk_f32_fp4 v[160:161], v17, 1.0
	v_pk_fma_f32 v[120:121], v[226:227], v[152:153], v[120:121] op_sel:[1,0,0] op_sel_hi:[1,1,1]
	v_cvt_scalef32_pk_f32_fp4 v[162:163], v17, 1.0 op_sel:[1,0,0]
	v_pk_fma_f32 v[122:123], v[226:227], v[154:155], v[122:123] op_sel:[1,0,0] op_sel_hi:[1,1,1]
	v_cvt_scalef32_pk_f32_fp4 v[152:153], v17, 1.0 op_sel:[0,1,0]
	v_pk_fma_f32 v[124:125], v[226:227], v[156:157], v[124:125] op_sel:[1,0,0] op_sel_hi:[1,1,1]
	v_cvt_scalef32_pk_f32_fp4 v[154:155], v17, 1.0 op_sel:[1,1,0]
	v_pk_fma_f32 v[126:127], v[226:227], v[158:159], v[126:127] op_sel:[1,0,0] op_sel_hi:[1,1,1]
	v_cvt_scalef32_pk_f32_fp4 v[156:157], v18, 1.0
	v_pk_fma_f32 v[128:129], v[226:227], v[160:161], v[128:129] op_sel:[1,0,0] op_sel_hi:[1,1,1]
	v_cvt_scalef32_pk_f32_fp4 v[158:159], v18, 1.0 op_sel:[1,0,0]
	v_pk_fma_f32 v[130:131], v[226:227], v[162:163], v[130:131] op_sel:[1,0,0] op_sel_hi:[1,1,1]
	v_cvt_scalef32_pk_f32_fp4 v[160:161], v18, 1.0 op_sel:[0,1,0]
	v_pk_fma_f32 v[132:133], v[226:227], v[152:153], v[132:133] op_sel:[1,0,0] op_sel_hi:[1,1,1]
	v_cvt_scalef32_pk_f32_fp4 v[162:163], v18, 1.0 op_sel:[1,1,0]
	v_pk_fma_f32 v[134:135], v[226:227], v[154:155], v[134:135] op_sel:[1,0,0] op_sel_hi:[1,1,1]
	v_cvt_scalef32_pk_f32_fp4 v[152:153], v19, 1.0
	v_pk_fma_f32 v[136:137], v[226:227], v[156:157], v[136:137] op_sel:[1,0,0] op_sel_hi:[1,1,1]
	v_cvt_scalef32_pk_f32_fp4 v[154:155], v19, 1.0 op_sel:[1,0,0]
	v_pk_fma_f32 v[138:139], v[226:227], v[158:159], v[138:139] op_sel:[1,0,0] op_sel_hi:[1,1,1]
	v_cvt_scalef32_pk_f32_fp4 v[156:157], v19, 1.0 op_sel:[0,1,0]
	v_pk_fma_f32 v[140:141], v[226:227], v[160:161], v[140:141] op_sel:[1,0,0] op_sel_hi:[1,1,1]
	v_cvt_scalef32_pk_f32_fp4 v[158:159], v19, 1.0 op_sel:[1,1,0]
	v_pk_fma_f32 v[142:143], v[226:227], v[162:163], v[142:143] op_sel:[1,0,0] op_sel_hi:[1,1,1]
	v_pk_fma_f32 v[144:145], v[226:227], v[152:153], v[144:145] op_sel:[1,0,0] op_sel_hi:[1,1,1]
	v_pk_fma_f32 v[146:147], v[226:227], v[154:155], v[146:147] op_sel:[1,0,0] op_sel_hi:[1,1,1]
	v_pk_fma_f32 v[148:149], v[226:227], v[156:157], v[148:149] op_sel:[1,0,0] op_sel_hi:[1,1,1]
	v_pk_fma_f32 v[150:151], v[226:227], v[158:159], v[150:151] op_sel:[1,0,0] op_sel_hi:[1,1,1]
	s_waitcnt vmcnt(7)
	v_cvt_scalef32_pk_f32_fp4 v[152:153], v12, 1.0
	v_cvt_scalef32_pk_f32_fp4 v[154:155], v12, 1.0 op_sel:[1,0,0]
	v_cvt_scalef32_pk_f32_fp4 v[156:157], v12, 1.0 op_sel:[0,1,0]
	v_cvt_scalef32_pk_f32_fp4 v[158:159], v12, 1.0 op_sel:[1,1,0]
	v_cvt_scalef32_pk_f32_fp4 v[160:161], v13, 1.0
	v_pk_fma_f32 v[120:121], v[228:229], v[152:153], v[120:121] op_sel_hi:[0,1,1]
	v_cvt_scalef32_pk_f32_fp4 v[162:163], v13, 1.0 op_sel:[1,0,0]
	v_pk_fma_f32 v[122:123], v[228:229], v[154:155], v[122:123] op_sel_hi:[0,1,1]
	v_cvt_scalef32_pk_f32_fp4 v[152:153], v13, 1.0 op_sel:[0,1,0]
	v_pk_fma_f32 v[124:125], v[228:229], v[156:157], v[124:125] op_sel_hi:[0,1,1]
	v_cvt_scalef32_pk_f32_fp4 v[154:155], v13, 1.0 op_sel:[1,1,0]
	v_pk_fma_f32 v[126:127], v[228:229], v[158:159], v[126:127] op_sel_hi:[0,1,1]
	v_cvt_scalef32_pk_f32_fp4 v[156:157], v14, 1.0
	v_pk_fma_f32 v[128:129], v[228:229], v[160:161], v[128:129] op_sel_hi:[0,1,1]
	v_cvt_scalef32_pk_f32_fp4 v[158:159], v14, 1.0 op_sel:[1,0,0]
	v_pk_fma_f32 v[130:131], v[228:229], v[162:163], v[130:131] op_sel_hi:[0,1,1]
	v_cvt_scalef32_pk_f32_fp4 v[160:161], v14, 1.0 op_sel:[0,1,0]
	v_pk_fma_f32 v[132:133], v[228:229], v[152:153], v[132:133] op_sel_hi:[0,1,1]
	v_cvt_scalef32_pk_f32_fp4 v[162:163], v14, 1.0 op_sel:[1,1,0]
	v_pk_fma_f32 v[134:135], v[228:229], v[154:155], v[134:135] op_sel_hi:[0,1,1]
	v_cvt_scalef32_pk_f32_fp4 v[152:153], v15, 1.0
	v_pk_fma_f32 v[136:137], v[228:229], v[156:157], v[136:137] op_sel_hi:[0,1,1]
	v_cvt_scalef32_pk_f32_fp4 v[154:155], v15, 1.0 op_sel:[1,0,0]
	v_pk_fma_f32 v[138:139], v[228:229], v[158:159], v[138:139] op_sel_hi:[0,1,1]
	v_cvt_scalef32_pk_f32_fp4 v[156:157], v15, 1.0 op_sel:[0,1,0]
	v_pk_fma_f32 v[140:141], v[228:229], v[160:161], v[140:141] op_sel_hi:[0,1,1]
	v_cvt_scalef32_pk_f32_fp4 v[158:159], v15, 1.0 op_sel:[1,1,0]
	v_pk_fma_f32 v[142:143], v[228:229], v[162:163], v[142:143] op_sel_hi:[0,1,1]
	v_pk_fma_f32 v[144:145], v[228:229], v[152:153], v[144:145] op_sel_hi:[0,1,1]
	v_pk_fma_f32 v[146:147], v[228:229], v[154:155], v[146:147] op_sel_hi:[0,1,1]
	v_pk_fma_f32 v[148:149], v[228:229], v[156:157], v[148:149] op_sel_hi:[0,1,1]
	v_pk_fma_f32 v[150:151], v[228:229], v[158:159], v[150:151] op_sel_hi:[0,1,1]
	s_waitcnt vmcnt(6)
; #define EV_LOADN(q_, g0_, n_) _Pragma("unroll") for (int k = 0; k < (n_); ++k) q_[k] = __builtin_bit_cast(uint4, __builtin_amdgcn_raw_buffer_load_b128(vrs, voff + si[((g0_) + k) * 8 + sub] * 128, 0, GATHER_AUX))
; #define EV_WAIT(n_) asm volatile("s_waitcnt vmcnt(" #n_ ")" ::: "memory")
; __device__ void phase_exp_v(KParams& p, char* smem) {
;     ...
;         EV_LOADN(qa, 0, 4); EV_LOADN(qb, 4, 4); EV_LOADN(qc, 8, 4); EV_LOADN(qd, 12, 4);
;         {
;           const int t1 = (tt + 1 < 16) ? t + 1 : t;
;           e0n = p.idx[(size_t)t1 * 128 + lane]; e1n = p.idx[(size_t)t1 * 128 + 64 + lane];
;           g0n = p.gate[(size_t)t1 * 128 + lane]; g1n = p.gate[(size_t)t1 * 128 + 64 + lane];
;         }
;         EV_WAIT(16); EV_COMPN(qa, 0, 4);
;         EV_WAIT(12); EV_COMPN(qb, 4, 4);
;         EV_WAIT(8); EV_COMPN(qc, 8, 4);
;         EV_WAIT(4); EV_COMPN(qd, 12, 4);
	v_cvt_scalef32_pk_f32_fp4 v[152:153], v8, 1.0
	v_cvt_scalef32_pk_f32_fp4 v[154:155], v8, 1.0 op_sel:[1,0,0]
	v_cvt_scalef32_pk_f32_fp4 v[156:157], v8, 1.0 op_sel:[0,1,0]
	v_cvt_scalef32_pk_f32_fp4 v[158:159], v8, 1.0 op_sel:[1,1,0]
	v_cvt_scalef32_pk_f32_fp4 v[160:161], v9, 1.0
	v_pk_fma_f32 v[120:121], v[228:229], v[152:153], v[120:121] op_sel:[1,0,0] op_sel_hi:[1,1,1]
	v_cvt_scalef32_pk_f32_fp4 v[162:163], v9, 1.0 op_sel:[1,0,0]
	v_pk_fma_f32 v[122:123], v[228:229], v[154:155], v[122:123] op_sel:[1,0,0] op_sel_hi:[1,1,1]
	v_cvt_scalef32_pk_f32_fp4 v[152:153], v9, 1.0 op_sel:[0,1,0]
	v_pk_fma_f32 v[124:125], v[228:229], v[156:157], v[124:125] op_sel:[1,0,0] op_sel_hi:[1,1,1]
	v_cvt_scalef32_pk_f32_fp4 v[154:155], v9, 1.0 op_sel:[1,1,0]
	v_pk_fma_f32 v[126:127], v[228:229], v[158:159], v[126:127] op_sel:[1,0,0] op_sel_hi:[1,1,1]
	v_cvt_scalef32_pk_f32_fp4 v[156:157], v10, 1.0
	v_pk_fma_f32 v[128:129], v[228:229], v[160:161], v[128:129] op_sel:[1,0,0] op_sel_hi:[1,1,1]
	v_cvt_scalef32_pk_f32_fp4 v[158:159], v10, 1.0 op_sel:[1,0,0]
	v_pk_fma_f32 v[130:131], v[228:229], v[162:163], v[130:131] op_sel:[1,0,0] op_sel_hi:[1,1,1]
	v_cvt_scalef32_pk_f32_fp4 v[160:161], v10, 1.0 op_sel:[0,1,0]
	v_pk_fma_f32 v[132:133], v[228:229], v[152:153], v[132:133] op_sel:[1,0,0] op_sel_hi:[1,1,1]
	v_cvt_scalef32_pk_f32_fp4 v[162:163], v10, 1.0 op_sel:[1,1,0]
	v_pk_fma_f32 v[134:135], v[228:229], v[154:155], v[134:135] op_sel:[1,0,0] op_sel_hi:[1,1,1]
	v_cvt_scalef32_pk_f32_fp4 v[152:153], v11, 1.0
	v_pk_fma_f32 v[136:137], v[228:229], v[156:157], v[136:137] op_sel:[1,0,0] op_sel_hi:[1,1,1]
	v_cvt_scalef32_pk_f32_fp4 v[154:155], v11, 1.0 op_sel:[1,0,0]
	v_pk_fma_f32 v[138:139], v[228:229], v[158:159], v[138:139] op_sel:[1,0,0] op_sel_hi:[1,1,1]
	v_cvt_scalef32_pk_f32_fp4 v[156:157], v11, 1.0 op_sel:[0,1,0]
	v_pk_fma_f32 v[140:141], v[228:229], v[160:161], v[140:141] op_sel:[1,0,0] op_sel_hi:[1,1,1]
	v_cvt_scalef32_pk_f32_fp4 v[158:159], v11, 1.0 op_sel:[1,1,0]
	v_pk_fma_f32 v[142:143], v[228:229], v[162:163], v[142:143] op_sel:[1,0,0] op_sel_hi:[1,1,1]
	v_pk_fma_f32 v[144:145], v[228:229], v[152:153], v[144:145] op_sel:[1,0,0] op_sel_hi:[1,1,1]
	v_pk_fma_f32 v[146:147], v[228:229], v[154:155], v[146:147] op_sel:[1,0,0] op_sel_hi:[1,1,1]
	v_pk_fma_f32 v[148:149], v[228:229], v[156:157], v[148:149] op_sel:[1,0,0] op_sel_hi:[1,1,1]
	v_pk_fma_f32 v[150:151], v[228:229], v[158:159], v[150:151] op_sel:[1,0,0] op_sel_hi:[1,1,1]
	s_waitcnt vmcnt(5)
	v_cvt_scalef32_pk_f32_fp4 v[152:153], v4, 1.0
	v_cvt_scalef32_pk_f32_fp4 v[154:155], v4, 1.0 op_sel:[1,0,0]
	v_cvt_scalef32_pk_f32_fp4 v[156:157], v4, 1.0 op_sel:[0,1,0]
	v_cvt_scalef32_pk_f32_fp4 v[158:159], v4, 1.0 op_sel:[1,1,0]
	v_cvt_scalef32_pk_f32_fp4 v[160:161], v5, 1.0
	v_pk_fma_f32 v[120:121], v[230:231], v[152:153], v[120:121] op_sel_hi:[0,1,1]
	v_cvt_scalef32_pk_f32_fp4 v[162:163], v5, 1.0 op_sel:[1,0,0]
	v_pk_fma_f32 v[122:123], v[230:231], v[154:155], v[122:123] op_sel_hi:[0,1,1]
	v_cvt_scalef32_pk_f32_fp4 v[152:153], v5, 1.0 op_sel:[0,1,0]
	v_pk_fma_f32 v[124:125], v[230:231], v[156:157], v[124:125] op_sel_hi:[0,1,1]
	v_cvt_scalef32_pk_f32_fp4 v[154:155], v5, 1.0 op_sel:[1,1,0]
	v_pk_fma_f32 v[126:127], v[230:231], v[158:159], v[126:127] op_sel_hi:[0,1,1]
	v_cvt_scalef32_pk_f32_fp4 v[156:157], v6, 1.0
	v_pk_fma_f32 v[128:129], v[230:231], v[160:161], v[128:129] op_sel_hi:[0,1,1]
	v_cvt_scalef32_pk_f32_fp4 v[158:159], v6, 1.0 op_sel:[1,0,0]
	v_pk_fma_f32 v[130:131], v[230:231], v[162:163], v[130:131] op_sel_hi:[0,1,1]
	v_cvt_scalef32_pk_f32_fp4 v[160:161], v6, 1.0 op_sel:[0,1,0]
	v_pk_fma_f32 v[132:133], v[230:231], v[152:153], v[132:133] op_sel_hi:[0,1,1]
	v_cvt_scalef32_pk_f32_fp4 v[162:163], v6, 1.0 op_sel:[1,1,0]
	v_pk_fma_f32 v[134:135], v[230:231], v[154:155], v[134:135] op_sel_hi:[0,1,1]
	v_cvt_scalef32_pk_f32_fp4 v[152:153], v7, 1.0
	v_pk_fma_f32 v[136:137], v[230:231], v[156:157], v[136:137] op_sel_hi:[0,1,1]
	v_cvt_scalef32_pk_f32_fp4 v[154:155], v7, 1.0 op_sel:[1,0,0]
	v_pk_fma_f32 v[138:139], v[230:231], v[158:159], v[138:139] op_sel_hi:[0,1,1]
	v_cvt_scalef32_pk_f32_fp4 v[156:157], v7, 1.0 op_sel:[0,1,0]
	v_pk_fma_f32 v[140:141], v[230:231], v[160:161], v[140:141] op_sel_hi:[0,1,1]
	v_cvt_scalef32_pk_f32_fp4 v[158:159], v7, 1.0 op_sel:[1,1,0]
	v_pk_fma_f32 v[142:143], v[230:231], v[162:163], v[142:143] op_sel_hi:[0,1,1]
	v_pk_fma_f32 v[144:145], v[230:231], v[152:153], v[144:145] op_sel_hi:[0,1,1]
	v_pk_fma_f32 v[146:147], v[230:231], v[154:155], v[146:147] op_sel_hi:[0,1,1]
	v_pk_fma_f32 v[148:149], v[230:231], v[156:157], v[148:149] op_sel_hi:[0,1,1]
	v_pk_fma_f32 v[150:151], v[230:231], v[158:159], v[150:151] op_sel_hi:[0,1,1]
	s_waitcnt vmcnt(4)
; __device__ void phase_exp_v(KParams& p, char* smem) {
;     ...
;         {
;           float* red = reinterpret_cast<float*>(smem + 8192) + w * 2304;
;           float* mr = red + (sub * 8 + cc) * 36;
; #pragma unroll
;           for (int q4 = 0; q4 < 8; ++q4)
;             *reinterpret_cast<float4*>(mr + q4 * 4) = float4{acc[q4 * 2].x, acc[q4 * 2].y, acc[q4 * 2 + 1].x, acc[q4 * 2 + 1].y};
;           __builtin_amdgcn_wave_barrier();
;           float4 r = *reinterpret_cast<const float4*>(red + (0 * 8 + sub) * 36 + cc * 4);
; #pragma unroll
;           for (int s8 = 1; s8 < 8; ++s8) {
;             const float4 r1 = *reinterpret_cast<const float4*>(red + (s8 * 8 + sub) * 36 + cc * 4);
;             r.x += r1.x; r.y += r1.y; r.z += r1.z; r.w += r1.w;
;           }
;           uint2 o4;
;           o4.x = pack2(r.x, r.y);
;           o4.y = pack2(r.z, r.w);
;           *reinterpret_cast<uint2*>(yfb + (size_t)t * D + x * 256 + sub * 32 + cc * 4) = o4;
	v_cvt_scalef32_pk_f32_fp4 v[152:153], v0, 1.0
	v_cvt_scalef32_pk_f32_fp4 v[154:155], v0, 1.0 op_sel:[1,0,0]
	v_cvt_scalef32_pk_f32_fp4 v[156:157], v0, 1.0 op_sel:[0,1,0]
	v_cvt_scalef32_pk_f32_fp4 v[158:159], v0, 1.0 op_sel:[1,1,0]
	v_cvt_scalef32_pk_f32_fp4 v[160:161], v1, 1.0
	v_pk_fma_f32 v[120:121], v[230:231], v[152:153], v[120:121] op_sel:[1,0,0] op_sel_hi:[1,1,1]
	v_cvt_scalef32_pk_f32_fp4 v[162:163], v1, 1.0 op_sel:[1,0,0]
	v_pk_fma_f32 v[122:123], v[230:231], v[154:155], v[122:123] op_sel:[1,0,0] op_sel_hi:[1,1,1]
	v_cvt_scalef32_pk_f32_fp4 v[152:153], v1, 1.0 op_sel:[0,1,0]
	v_pk_fma_f32 v[124:125], v[230:231], v[156:157], v[124:125] op_sel:[1,0,0] op_sel_hi:[1,1,1]
	v_cvt_scalef32_pk_f32_fp4 v[154:155], v1, 1.0 op_sel:[1,1,0]
	v_pk_fma_f32 v[126:127], v[230:231], v[158:159], v[126:127] op_sel:[1,0,0] op_sel_hi:[1,1,1]
	v_cvt_scalef32_pk_f32_fp4 v[156:157], v2, 1.0
	v_pk_fma_f32 v[128:129], v[230:231], v[160:161], v[128:129] op_sel:[1,0,0] op_sel_hi:[1,1,1]
	v_cvt_scalef32_pk_f32_fp4 v[158:159], v2, 1.0 op_sel:[1,0,0]
	v_pk_fma_f32 v[130:131], v[230:231], v[162:163], v[130:131] op_sel:[1,0,0] op_sel_hi:[1,1,1]
	v_cvt_scalef32_pk_f32_fp4 v[160:161], v2, 1.0 op_sel:[0,1,0]
	v_pk_fma_f32 v[132:133], v[230:231], v[152:153], v[132:133] op_sel:[1,0,0] op_sel_hi:[1,1,1]
	v_cvt_scalef32_pk_f32_fp4 v[162:163], v2, 1.0 op_sel:[1,1,0]
	v_pk_fma_f32 v[134:135], v[230:231], v[154:155], v[134:135] op_sel:[1,0,0] op_sel_hi:[1,1,1]
	v_cvt_scalef32_pk_f32_fp4 v[152:153], v3, 1.0
	v_pk_fma_f32 v[136:137], v[230:231], v[156:157], v[136:137] op_sel:[1,0,0] op_sel_hi:[1,1,1]
	v_cvt_scalef32_pk_f32_fp4 v[154:155], v3, 1.0 op_sel:[1,0,0]
	v_pk_fma_f32 v[138:139], v[230:231], v[158:159], v[138:139] op_sel:[1,0,0] op_sel_hi:[1,1,1]
	v_cvt_scalef32_pk_f32_fp4 v[156:157], v3, 1.0 op_sel:[0,1,0]
	v_pk_fma_f32 v[140:141], v[230:231], v[160:161], v[140:141] op_sel:[1,0,0] op_sel_hi:[1,1,1]
	v_cvt_scalef32_pk_f32_fp4 v[158:159], v3, 1.0 op_sel:[1,1,0]
	v_pk_fma_f32 v[142:143], v[230:231], v[162:163], v[142:143] op_sel:[1,0,0] op_sel_hi:[1,1,1]
	v_pk_fma_f32 v[144:145], v[230:231], v[152:153], v[144:145] op_sel:[1,0,0] op_sel_hi:[1,1,1]
	v_pk_fma_f32 v[146:147], v[230:231], v[154:155], v[146:147] op_sel:[1,0,0] op_sel_hi:[1,1,1]
	v_pk_fma_f32 v[148:149], v[230:231], v[156:157], v[148:149] op_sel:[1,0,0] op_sel_hi:[1,1,1]
	v_pk_fma_f32 v[150:151], v[230:231], v[158:159], v[150:151] op_sel:[1,0,0] op_sel_hi:[1,1,1]
	v_and_b32_e32 v170, 8, v44
	s_nop 0
	v_permlane32_swap_b32_e32 v120, v136
	v_permlane32_swap_b32_e32 v121, v137
	v_permlane32_swap_b32_e32 v122, v138
	v_permlane32_swap_b32_e32 v123, v139
	v_permlane32_swap_b32_e32 v124, v140
	v_permlane32_swap_b32_e32 v125, v141
	v_permlane32_swap_b32_e32 v126, v142
	v_permlane32_swap_b32_e32 v127, v143
	v_permlane32_swap_b32_e32 v128, v144
	v_permlane32_swap_b32_e32 v129, v145
	v_permlane32_swap_b32_e32 v130, v146
	v_permlane32_swap_b32_e32 v131, v147
	v_permlane32_swap_b32_e32 v132, v148
	v_permlane32_swap_b32_e32 v133, v149
	v_permlane32_swap_b32_e32 v134, v150
	v_permlane32_swap_b32_e32 v135, v151
	v_pk_add_f32 v[120:121], v[120:121], v[136:137]
	v_pk_add_f32 v[122:123], v[122:123], v[138:139]
	v_pk_add_f32 v[124:125], v[124:125], v[140:141]
	v_pk_add_f32 v[126:127], v[126:127], v[142:143]
	v_pk_add_f32 v[128:129], v[128:129], v[144:145]
	v_pk_add_f32 v[130:131], v[130:131], v[146:147]
	v_pk_add_f32 v[132:133], v[132:133], v[148:149]
	v_pk_add_f32 v[134:135], v[134:135], v[150:151]
	v_cmp_ne_u32_e32 vcc, 0, v170
	s_nop 0
	v_permlane16_swap_b32_e32 v120, v128
	v_permlane16_swap_b32_e32 v121, v129
	v_permlane16_swap_b32_e32 v122, v130
	v_permlane16_swap_b32_e32 v123, v131
	v_permlane16_swap_b32_e32 v124, v132
	v_permlane16_swap_b32_e32 v125, v133
	v_permlane16_swap_b32_e32 v126, v134
	v_permlane16_swap_b32_e32 v127, v135
	v_pk_add_f32 v[120:121], v[120:121], v[128:129]
	v_pk_add_f32 v[122:123], v[122:123], v[130:131]
	v_pk_add_f32 v[124:125], v[124:125], v[132:133]
	v_pk_add_f32 v[126:127], v[126:127], v[134:135]
	s_nop 1
	v_add_f32_dpp v136, v120, v120 row_ror:8 row_mask:0xf bank_mask:0xf
	v_add_f32_dpp v137, v121, v121 row_ror:8 row_mask:0xf bank_mask:0xf
	v_add_f32_dpp v138, v122, v122 row_ror:8 row_mask:0xf bank_mask:0xf
	v_add_f32_dpp v139, v123, v123 row_ror:8 row_mask:0xf bank_mask:0xf
	v_add_f32_dpp v140, v124, v124 row_ror:8 row_mask:0xf bank_mask:0xf
	v_add_f32_dpp v141, v125, v125 row_ror:8 row_mask:0xf bank_mask:0xf
	v_add_f32_dpp v142, v126, v126 row_ror:8 row_mask:0xf bank_mask:0xf
	v_add_f32_dpp v143, v127, v127 row_ror:8 row_mask:0xf bank_mask:0xf
	v_cndmask_b32_e32 v136, v136, v140, vcc
	v_cndmask_b32_e32 v137, v137, v141, vcc
	v_cndmask_b32_e32 v138, v138, v142, vcc
	v_cndmask_b32_e32 v139, v139, v143, vcc
	v_cvt_pk_bf16_f32 v0, v136, v137
	v_cvt_pk_bf16_f32 v1, v138, v139
	v_lshl_add_u64 v[2:3], v[52:53], 0, s[18:19]
	s_add_u32 s18, s18, 0x1000
	v_add_co_u32_e32 v2, vcc, s14, v2
	s_addc_u32 s19, s19, 0
	s_nop 0
	v_addc_co_u32_e32 v3, vcc, 0, v3, vcc
	s_cmp_eq_u32 s18, 0x10000
	global_store_dwordx2 v[2:3], v[0:1], off
	s_cbranch_scc0 .LBB0_1393
	s_branch .LBB0_1381
